# plus attention pool-entry selected-key index loads issued together
# baseline (speedup 1.0000x reference)
.LBB0_535:
	s_or_b64 exec, exec, s[0:1]
	s_and_b64 s[0:1], s[54:55], exec
	s_movk_i32 s0, 0x1fff
	s_cselect_b32 s59, 0x3fff, s0
	s_sub_i32 s56, s59, s58
	s_mov_b32 s57, s5
	s_lshl_b64 s[0:1], s[56:57], 9
	v_lshl_add_u64 v[0:1], v[144:145], 0, s[0:1]
	global_load_ushort v2, v[0:1], off
	global_load_ushort v5, v[0:1], off offset:128
	global_load_ushort v6, v[0:1], off offset:256
	global_load_ushort v7, v[0:1], off offset:384
	s_lshl_b32 s6, s30, 9
	s_mul_i32 s0, s56, 0x1100
	v_add_u32_e32 v183, s6, v163
	s_waitcnt vmcnt(0)
	v_mov_b32_e32 v4, 0
	v_mov_b32_e32 v3, 0
	ds_write_b16 v162, v2 offset:18432
	ds_write_b16 v162, v5 offset:18560
	ds_write_b16 v162, v6 offset:18688
	ds_write_b16 v162, v7 offset:18816
	v_mov_b32_e32 v1, 0
	v_mov_b32_e32 v2, 0
	v_add_u32_e32 v0, s0, v183
	v_lshl_add_u32 v16, v0, 1, v164
	v_mov_b32_e32 v0, 0
	s_and_saveexec_b64 s[0:1], s[38:39]
	s_cbranch_execz .LBB0_537
	global_load_dwordx4 v[0:3], v16, s[44:45]
